# speedup vs baseline: 1.0011x; 1.0011x over previous
.LBB2_4:
	s_or_b64 exec, exec, s[8:9]
	s_lshr_b32 s41, s43, 6
	v_bfe_u32 v1, v0, 4, 2
	s_lshl_b32 s45, s41, 2
	v_or_b32_e32 v41, s45, v1
	v_lshlrev_b32_e32 v2, 2, v41
	s_waitcnt lgkmcnt(0)
	s_barrier
	ds_read_b32 v2, v2 offset:25152
	s_and_b32 s44, s21, 0xffff
	v_and_b32_e32 v68, 63, v0
	s_mov_b32 s23, 0x20000
	s_mov_b32 s22, 0x4e2000
	s_waitcnt lgkmcnt(0)
	v_add_u32_e32 v34, s33, v2
	v_lshlrev_b32_e32 v3, 2, v2
	ds_read_b32 v36, v3 offset:16640
	ds_read_b32 v35, v3 offset:25088
	s_mov_b64 s[2:3], -1
	s_waitcnt lgkmcnt(0)
	v_add_u32_e32 v37, v36, v35
	v_cmp_gt_i32_e32 vcc, 48, v35
	s_cmp_eq_u64 vcc, exec
	s_cbranch_scc0 .Ll1_generic

.Ll1_generic:
	v_mov_b32_e32 v7, 0
	v_lshlrev_b32_e32 v8, 2, v68
	v_mov_b32_e32 v9, v7
	v_lshl_add_u64 v[10:11], s[20:21], 0, v[8:9]
	s_mov_b32 s46, 0
	s_branch .LBB2_7

.LBB2_24:
	s_load_dwordx2 s[14:15], s[0:1], 0x48
	s_mov_b64 s[2:3], 0
	s_branch .LBB2_25
	s_nop 0
	s_nop 0
	s_nop 0
	s_nop 0
	s_nop 0
	s_nop 0
	s_nop 0
	s_nop 0
	s_nop 0
	s_nop 0
	s_nop 0
	s_nop 0
	s_nop 0
	s_endpgm

.LBB3_4:
	s_endpgm
.LBB3_22:
	v_add_u32_e32 v8, v7, v33
	v_cmp_lt_i32_e64 s[0:1], v33, v37
	v_or_b32_e32 v24, 16, v33
	v_or_b32_e32 v21, 32, v33
	v_ashrrev_i32_e32 v9, 31, v8
	v_cmp_lt_i32_e64 s[2:3], v24, v37
	v_cmp_lt_i32_e64 s[4:5], v21, v37
	v_lshl_add_u64 v[26:27], v[8:9], 4, s[6:7]
	v_mov_b32_e32 v15, v6
	v_mov_b32_e32 v17, 0
	v_mov_b32_e32 v10, v6
	v_mov_b32_e32 v13, 0
	v_mov_b32_e32 v9, 0
	s_mov_b64 s[16:17], exec
	s_mov_b64 exec, s[0:1]
	s_cbranch_execz .Ll2_csr1
	global_load_dwordx4 v[14:17], v[26:27], off nt

.LBB3_55:
	s_waitcnt vmcnt(1)
	v_add_f32_e32 v7, v8, v14
	v_add_f32_e32 v7, v13, v7
	v_mul_f32_e32 v14, 0x3e4ccccd, v7
	v_cmp_lt_f32_e32 vcc, 0, v7
	s_nop 1
	v_cndmask_b32_e32 v7, v14, v7, vcc
	s_or_b64 exec, exec, s[6:7]
	v_mov_b32_e32 v14, 0xff800000
	s_and_saveexec_b64 s[6:7], s[4:5]
	s_cbranch_execnz .LBB3_31
	s_branch .LBB3_32
.LBB3_5:
	s_waitcnt vmcnt(0)
	v_pk_add_f32 v[0:1], v[40:41], v[44:45]
	v_pk_add_f32 v[18:19], v[42:43], v[46:47]
	v_mbcnt_hi_u32_b32 v8, -1, v32
	v_and_b32_e32 v13, 64, v8
	v_xor_b32_e32 v12, 16, v8
	v_add_u32_e32 v13, 64, v13
	v_cmp_lt_i32_e32 vcc, v12, v13
	v_mov_b32_e32 v9, 0
	v_mov_b32_e32 v21, v9
	v_cndmask_b32_e32 v12, v8, v12, vcc
	v_lshlrev_b32_e32 v34, 2, v12
	v_xor_b32_e32 v12, 32, v8
	v_cmp_lt_i32_e32 vcc, v12, v13
	v_lshlrev_b32_e32 v14, 2, v36
	s_movk_i32 s2, 0x100
	v_cndmask_b32_e32 v12, v8, v12, vcc
	v_lshlrev_b32_e32 v8, 2, v8
	v_lshl_add_u64 v[10:11], s[16:17], 0, v[20:21]
	s_mov_b32 s23, 0
	v_lshlrev_b32_e32 v35, 2, v12
	s_waitcnt lgkmcnt(0)
	v_lshl_add_u64 v[12:13], s[8:9], 0, v[20:21]
	v_and_or_b32 v21, v8, s2, v14
	s_branch .LBB3_7

.LBB3_21:
	s_branch .LBB3_4
	s_nop 0
	s_nop 0
	s_nop 0
	s_nop 0
	s_nop 0
	s_nop 0
	s_nop 0
	s_nop 0
	s_nop 0
	s_endpgm
